# EpiBf16 epilogues (input bf16 + gate GEMMs): per-tile row-factor loads hoisted to tile start, reloaded only when the row block changes; epilogue load waits removed
# speedup vs baseline: 1.0032x; 1.0021x over previous
.LBB0_182:
	s_cmpk_gt_i32 s2, 0x63f
	v_readfirstlane_b32 s9, v1
	s_cbranch_scc1 .LBB0_198
	s_mov_b32 s101, -1
	v_writelane_b32 v255, s101, 12
	v_lshlrev_b32_e32 v2, 4, v1
	v_add_u32_e32 v4, 0x2000, v2
	v_ashrrev_i32_e32 v5, 31, v4
	v_lshrrev_b32_e32 v5, 22, v5
	v_add_u32_e32 v5, v4, v5
	v_ashrrev_i32_e32 v12, 10, v5
	v_mul_i32_i24_e32 v5, 0x400, v12
	v_sub_u32_e32 v4, v4, v5
	v_lshrrev_b32_e32 v5, 4, v4
	v_bitop3_b32 v4, v5, v4, 32 bitop3:0x6c
	v_ashrrev_i32_e32 v5, 31, v4
	v_lshrrev_b32_e32 v5, 26, v5
	v_add_u32_e32 v5, v4, v5
	v_lshlrev_b32_e32 v6, 3, v12
	v_ashrrev_i32_e32 v13, 6, v5
	v_and_b32_e32 v6, -16, v6
	v_add_u32_e32 v6, v13, v6
	v_and_b32_e32 v7, 3, v13
	s_mov_b32 s0, 0xfffe0
	v_lshrrev_b32_e32 v8, 2, v6
	v_lshlrev_b32_e32 v9, 1, v6
	v_and_b32_e32 v5, 0xc0, v5
	v_and_or_b32 v7, v6, s0, v7
	v_and_b32_e32 v8, 4, v8
	v_and_b32_e32 v9, 24, v9
	v_sub_u32_e32 v4, v4, v5
	v_or3_b32 v7, v7, v8, v9
	v_lshlrev_b32_e32 v8, 5, v12
	v_ashrrev_i16_sdwa v4, v228, sext(v4) dst_sel:DWORD dst_unused:UNUSED_PAD src0_sel:DWORD src1_sel:BYTE_0
	v_and_b32_e32 v8, 32, v8
	v_bfe_i32 v14, v4, 0, 16
	v_add_lshl_u32 v4, v8, v14, 1
	s_waitcnt vmcnt(0)
	v_lshl_add_u32 v132, v7, 12, v4
	v_lshl_add_u32 v134, v6, 12, v4
	v_bfe_i32 v4, v1, 27, 1
	v_lshrrev_b32_e32 v4, 22, v4
	v_add_u32_e32 v4, v2, v4
	v_and_b32_e32 v4, 0xfffffc00, v4
	v_sub_u32_e32 v2, v2, v4
	v_lshrrev_b32_e32 v4, 4, v2
	v_ashrrev_i32_e32 v5, 31, v1
	v_bitop3_b32 v2, v4, v2, 32 bitop3:0x6c
	v_lshrrev_b32_e32 v5, 26, v5
	v_ashrrev_i32_e32 v4, 31, v2
	v_add_u32_e32 v5, v1, v5
	v_lshrrev_b32_e32 v4, 26, v4
	v_ashrrev_i32_e32 v16, 6, v5
	s_add_u32 s26, s6, 0x5000000
	v_add_u32_e32 v4, v2, v4
	v_lshlrev_b32_e32 v5, 3, v16
	s_addc_u32 s27, s7, 0
	v_ashrrev_i32_e32 v15, 6, v4
	v_and_b32_e32 v5, -16, v5
	s_add_u32 s30, s6, 0x400000
	v_add_u32_e32 v5, v15, v5
	v_and_b32_e32 v6, 3, v15
	s_addc_u32 s31, s7, 0
	v_and_or_b32 v6, v5, s0, v6
	s_ashr_i32 s0, s2, 31
	s_lshr_b32 s0, s0, 29
	s_add_i32 s0, s2, s0
	s_ashr_i32 s11, s9, 6
	s_ashr_i32 s1, s0, 3
	s_and_b32 s0, s0, -8
	s_ashr_i32 s12, s9, 8
	s_lshl_b32 s10, s11, 10
	s_sub_i32 s0, s2, s0
	s_cmp_lt_i32 s0, 0
	s_movk_i32 s8, 0xc9
	s_cselect_b32 s8, s8, 0xc8
	s_mul_i32 s0, s8, s0
	s_add_i32 s0, s0, s1
	s_mul_hi_i32 s1, s0, 0x51eb851f
	s_lshr_b32 s8, s1, 31
	s_ashr_i32 s1, s1, 6
	s_add_i32 s1, s1, s8
	s_lshl_b32 s13, s1, 3
	s_mulk_i32 s1, 0xc8
	s_sub_i32 s0, s0, s1
	s_bfe_u32 s1, s0, 0x3001c
	s_add_i32 s1, s0, s1
	s_sext_i32_i16 s8, s1
	s_and_b32 s1, s1, 0xfff8
	s_sub_i32 s0, s0, s1
	s_sext_i32_i16 s0, s0
	s_lshr_b32 s8, s8, 3
	s_add_i32 s18, s13, s0
	s_ashr_i32 s19, s18, 31
	s_bfe_i64 s[14:15], s[8:9], 0x100000
	s_lshl_b64 s[0:1], s[18:19], 20
	s_lshl_b64 s[14:15], s[14:15], 20
	s_add_u32 s20, s30, s14
	s_addc_u32 s21, s31, s15
	s_add_i32 s33, s72, 0x10000
	v_lshrrev_b32_e32 v7, 2, v5
	v_lshlrev_b32_e32 v8, 1, v5
	v_and_b32_e32 v4, 0xc0, v4
	s_add_i32 s34, s33, s10
	v_and_b32_e32 v7, 4, v7
	v_and_b32_e32 v8, 24, v8
	v_sub_u32_e32 v2, v2, v4
	s_add_i32 s35, s34, 0x2000
	v_or3_b32 v6, v6, v7, v8
	v_lshlrev_b32_e32 v7, 5, v16
	v_ashrrev_i16_sdwa v2, v228, sext(v2) dst_sel:DWORD dst_unused:UNUSED_PAD src0_sel:DWORD src1_sel:BYTE_0
	s_add_u32 s14, s20, 0x80000
	v_and_b32_e32 v7, 32, v7
	v_bfe_i32 v17, v2, 0, 16
	s_addc_u32 s15, s21, 0
	s_add_i32 s38, s72, 0x14000
	v_add_lshl_u32 v4, v7, v17, 1
	s_add_i32 s39, s38, s10
	v_lshl_add_u32 v2, v6, 12, v4
	s_mov_b32 m0, s34
	s_add_i32 s40, s39, 0x2000
	global_load_lds_dwordx4 v2, s[20:21]
	s_mov_b32 m0, s35
	s_add_u32 s22, s26, s0
	global_load_lds_dwordx4 v132, s[20:21]
	s_mov_b32 m0, s39
	s_addc_u32 s23, s27, s1
	s_add_i32 s41, s72, s10
	global_load_lds_dwordx4 v2, s[14:15]
	s_mov_b32 m0, s40
	s_add_i32 s42, s41, 0x2000
	v_lshl_add_u32 v136, v5, 12, v4
	global_load_lds_dwordx4 v132, s[14:15]
	s_mov_b32 m0, s41
	s_add_u32 s0, s22, 0x80000
	global_load_lds_dwordx4 v136, s[22:23]
	s_mov_b32 m0, s42
	s_addc_u32 s1, s23, 0
	s_add_i32 s43, s41, 0x4000
	global_load_lds_dwordx4 v134, s[22:23]
	s_mov_b32 m0, s43
	s_add_i32 s44, s41, 0x6000
	global_load_lds_dwordx4 v136, s[0:1]
	s_mov_b32 m0, s44
	v_mov_b32_e32 v133, v3
	global_load_lds_dwordx4 v134, s[0:1]
	v_mov_b32_e32 v137, v3
	v_mov_b32_e32 v135, v3
	s_cmp_eq_u32 s12, 1
	v_lshl_add_u64 v[10:11], s[20:21], 0, v[2:3]
	v_lshl_add_u64 v[8:9], s[20:21], 0, v[132:133]
	v_lshl_add_u64 v[4:5], s[22:23], 0, v[136:137]
	s_cselect_b64 s[0:1], -1, 0
	s_cmp_lg_u32 s12, 1
	v_lshl_add_u64 v[6:7], s[22:23], 0, v[134:135]
	s_cbranch_scc1 .LBB0_185
	s_barrier

.LBB0_188:
	v_readlane_b32 s100, v255, 12
	s_cmp_eq_u32 s100, s18
	s_cbranch_scc1 .Lrf_have_in
	v_writelane_b32 v255, s18, 12
	v_lshl_add_u32 v246, s18, 8, v151
	v_ashrrev_i32_e32 v247, 31, v246
	v_lshl_add_u64 v[246:247], v[246:247], 2, s[4:5]
	global_load_dword v222, v[246:247], off
	global_load_dword v224, v[246:247], off offset:64
	global_load_dword v232, v[246:247], off offset:128
	global_load_dword v234, v[246:247], off offset:192
	global_load_dword v236, v[246:247], off offset:512
	global_load_dword v238, v[246:247], off offset:576
	global_load_dword v242, v[246:247], off offset:640
	global_load_dword v244, v[246:247], off offset:704

.LBB0_194:
	v_lshl_add_u32 v146, s18, 8, v151
	v_ashrrev_i32_e32 v147, 31, v146
	v_lshl_add_u64 v[148:149], v[146:147], 2, s[4:5]
	v_lshl_or_b32 v144, s19, 8, v153
	v_ashrrev_i32_e32 v145, 31, v144
	v_mov_b64_e32 v[142:143], s[6:7]
	s_movk_i32 s24, 0x7200
	v_mad_i64_i32 v[158:159], s[18:19], v146, s24, v[142:143]
	v_lshlrev_b64 v[144:145], 1, v[144:145]
	v_lshl_add_u64 v[158:159], v[158:159], 0, v[144:145]
	s_andn2_b64 vcc, exec, s[36:37]
	s_mov_b32 s25, 0x800000
	s_waitcnt lgkmcnt(0)
	v_pk_mul_f32 v[114:115], v[114:115], v[224:225] op_sel_hi:[1,0]
	v_pk_mul_f32 v[106:107], v[106:107], v[224:225] op_sel_hi:[1,0]
	v_pk_mul_f32 v[98:99], v[98:99], v[232:233] op_sel_hi:[1,0]
	v_pk_mul_f32 v[162:163], v[126:127], v[222:223] op_sel_hi:[1,0]
	v_pk_mul_f32 v[126:127], v[124:125], v[222:223] op_sel_hi:[1,0]
	v_pk_mul_f32 v[130:131], v[130:131], v[222:223] op_sel_hi:[1,0]
	v_pk_mul_f32 v[124:125], v[128:129], v[222:223] op_sel_hi:[1,0]
	v_cvt_pk_bf16_f32 v126, v126, v127
	v_cvt_pk_bf16_f32 v124, v124, v125
	v_cvt_pk_bf16_f32 v125, v130, v131
	v_cvt_pk_bf16_f32 v127, v162, v163
	global_store_dwordx4 v[158:159], v[124:127], off
	v_pk_mul_f32 v[122:123], v[122:123], v[222:223] op_sel_hi:[1,0]
	v_pk_mul_f32 v[90:91], v[90:91], v[232:233] op_sel_hi:[1,0]
	v_pk_mul_f32 v[124:125], v[118:119], v[222:223] op_sel_hi:[1,0]
	v_pk_mul_f32 v[118:119], v[116:117], v[222:223] op_sel_hi:[1,0]
	v_pk_mul_f32 v[116:117], v[120:121], v[222:223] op_sel_hi:[1,0]
	v_cvt_pk_bf16_f32 v118, v118, v119
	v_cvt_pk_bf16_f32 v116, v116, v117
	v_cvt_pk_bf16_f32 v117, v122, v123
	v_cvt_pk_bf16_f32 v119, v124, v125
	global_store_dwordx4 v[158:159], v[116:119], off offset:256
	v_pk_mul_f32 v[82:83], v[82:83], v[234:235] op_sel_hi:[1,0]
	v_pk_mul_f32 v[74:75], v[74:75], v[234:235] op_sel_hi:[1,0]
	v_or_b32_e32 v116, 16, v146
	v_mad_i64_i32 v[116:117], s[18:19], v116, s24, v[142:143]
	v_pk_mul_f32 v[118:119], v[110:111], v[224:225] op_sel_hi:[1,0]
	v_pk_mul_f32 v[110:111], v[108:109], v[224:225] op_sel_hi:[1,0]
	v_pk_mul_f32 v[108:109], v[112:113], v[224:225] op_sel_hi:[1,0]
	v_lshl_add_u64 v[116:117], v[116:117], 0, v[144:145]
	v_cvt_pk_bf16_f32 v108, v108, v109
	v_cvt_pk_bf16_f32 v109, v114, v115
	v_cvt_pk_bf16_f32 v110, v110, v111
	v_cvt_pk_bf16_f32 v111, v118, v119
	global_store_dwordx4 v[116:117], v[108:111], off
	s_nop 1
	v_pk_mul_f32 v[108:109], v[102:103], v[224:225] op_sel_hi:[1,0]
	v_pk_mul_f32 v[102:103], v[100:101], v[224:225] op_sel_hi:[1,0]
	v_pk_mul_f32 v[100:101], v[104:105], v[224:225] op_sel_hi:[1,0]
	v_cvt_pk_bf16_f32 v102, v102, v103
	v_cvt_pk_bf16_f32 v100, v100, v101
	v_cvt_pk_bf16_f32 v101, v106, v107
	v_cvt_pk_bf16_f32 v103, v108, v109
	global_store_dwordx4 v[116:117], v[100:103], off offset:256
	s_nop 1
	v_or_b32_e32 v100, 32, v146
	v_mad_i64_i32 v[100:101], s[18:19], v100, s24, v[142:143]
	v_pk_mul_f32 v[102:103], v[94:95], v[232:233] op_sel_hi:[1,0]
	v_pk_mul_f32 v[94:95], v[92:93], v[232:233] op_sel_hi:[1,0]
	v_pk_mul_f32 v[92:93], v[96:97], v[232:233] op_sel_hi:[1,0]
	v_lshl_add_u64 v[100:101], v[100:101], 0, v[144:145]
	v_cvt_pk_bf16_f32 v92, v92, v93
	v_cvt_pk_bf16_f32 v93, v98, v99
	v_cvt_pk_bf16_f32 v94, v94, v95
	v_cvt_pk_bf16_f32 v95, v102, v103
	global_store_dwordx4 v[100:101], v[92:95], off
	s_nop 1
	v_pk_mul_f32 v[92:93], v[86:87], v[232:233] op_sel_hi:[1,0]
	v_pk_mul_f32 v[86:87], v[84:85], v[232:233] op_sel_hi:[1,0]
	v_pk_mul_f32 v[84:85], v[88:89], v[232:233] op_sel_hi:[1,0]
	v_cvt_pk_bf16_f32 v86, v86, v87
	v_cvt_pk_bf16_f32 v84, v84, v85
	v_cvt_pk_bf16_f32 v85, v90, v91
	v_cvt_pk_bf16_f32 v87, v92, v93
	global_store_dwordx4 v[100:101], v[84:87], off offset:256
	s_nop 1
	v_or_b32_e32 v84, 48, v146
	v_mad_i64_i32 v[84:85], s[18:19], v84, s24, v[142:143]
	v_pk_mul_f32 v[86:87], v[78:79], v[234:235] op_sel_hi:[1,0]
	v_pk_mul_f32 v[78:79], v[76:77], v[234:235] op_sel_hi:[1,0]
	v_pk_mul_f32 v[76:77], v[80:81], v[234:235] op_sel_hi:[1,0]
	v_lshl_add_u64 v[84:85], v[84:85], 0, v[144:145]
	v_cvt_pk_bf16_f32 v76, v76, v77
	v_cvt_pk_bf16_f32 v77, v82, v83
	v_cvt_pk_bf16_f32 v78, v78, v79
	v_cvt_pk_bf16_f32 v79, v86, v87
	global_store_dwordx4 v[84:85], v[76:79], off
	s_nop 1
	v_pk_mul_f32 v[76:77], v[70:71], v[234:235] op_sel_hi:[1,0]
	v_pk_mul_f32 v[70:71], v[68:69], v[234:235] op_sel_hi:[1,0]
	v_pk_mul_f32 v[68:69], v[72:73], v[234:235] op_sel_hi:[1,0]
	v_cvt_pk_bf16_f32 v70, v70, v71
	v_cvt_pk_bf16_f32 v68, v68, v69
	v_cvt_pk_bf16_f32 v69, v74, v75
	v_cvt_pk_bf16_f32 v71, v76, v77
	global_store_dwordx4 v[84:85], v[68:71], off offset:256
	s_nop 0
	v_add_u32_e32 v69, 0x80, v146
	v_mad_i64_i32 v[74:75], s[18:19], v69, s24, v[142:143]
	v_lshl_add_u64 v[74:75], v[74:75], 0, v[144:145]
	s_waitcnt lgkmcnt(0)
	v_pk_mul_f32 v[50:51], v[50:51], v[238:239] op_sel_hi:[1,0]
	v_pk_mul_f32 v[42:43], v[42:43], v[238:239] op_sel_hi:[1,0]
	v_pk_mul_f32 v[34:35], v[34:35], v[242:243] op_sel_hi:[1,0]
	v_pk_mul_f32 v[78:79], v[62:63], v[236:237] op_sel_hi:[1,0]
	v_pk_mul_f32 v[62:63], v[60:61], v[236:237] op_sel_hi:[1,0]
	v_pk_mul_f32 v[66:67], v[66:67], v[236:237] op_sel_hi:[1,0]
	v_pk_mul_f32 v[60:61], v[64:65], v[236:237] op_sel_hi:[1,0]
	v_cvt_pk_bf16_f32 v62, v62, v63
	v_cvt_pk_bf16_f32 v60, v60, v61
	v_cvt_pk_bf16_f32 v61, v66, v67
	v_cvt_pk_bf16_f32 v63, v78, v79
	global_store_dwordx4 v[74:75], v[60:63], off
	v_pk_mul_f32 v[58:59], v[58:59], v[236:237] op_sel_hi:[1,0]
	v_pk_mul_f32 v[26:27], v[26:27], v[242:243] op_sel_hi:[1,0]
	v_pk_mul_f32 v[60:61], v[54:55], v[236:237] op_sel_hi:[1,0]
	v_pk_mul_f32 v[54:55], v[52:53], v[236:237] op_sel_hi:[1,0]
	v_pk_mul_f32 v[52:53], v[56:57], v[236:237] op_sel_hi:[1,0]
	v_cvt_pk_bf16_f32 v54, v54, v55
	v_cvt_pk_bf16_f32 v52, v52, v53
	v_cvt_pk_bf16_f32 v53, v58, v59
	v_cvt_pk_bf16_f32 v55, v60, v61
	global_store_dwordx4 v[74:75], v[52:55], off offset:256
	v_pk_mul_f32 v[18:19], v[18:19], v[244:245] op_sel_hi:[1,0]
	v_pk_mul_f32 v[10:11], v[10:11], v[244:245] op_sel_hi:[1,0]
	v_add_u32_e32 v52, 0x90, v146
	v_mad_i64_i32 v[52:53], s[18:19], v52, s24, v[142:143]
	v_pk_mul_f32 v[54:55], v[46:47], v[238:239] op_sel_hi:[1,0]
	v_pk_mul_f32 v[46:47], v[44:45], v[238:239] op_sel_hi:[1,0]
	v_pk_mul_f32 v[44:45], v[48:49], v[238:239] op_sel_hi:[1,0]
	v_lshl_add_u64 v[52:53], v[52:53], 0, v[144:145]
	v_cvt_pk_bf16_f32 v44, v44, v45
	v_cvt_pk_bf16_f32 v45, v50, v51
	v_cvt_pk_bf16_f32 v46, v46, v47
	v_cvt_pk_bf16_f32 v47, v54, v55
	global_store_dwordx4 v[52:53], v[44:47], off
	s_nop 1
	v_pk_mul_f32 v[44:45], v[38:39], v[238:239] op_sel_hi:[1,0]
	v_pk_mul_f32 v[38:39], v[36:37], v[238:239] op_sel_hi:[1,0]
	v_pk_mul_f32 v[36:37], v[40:41], v[238:239] op_sel_hi:[1,0]
	v_cvt_pk_bf16_f32 v38, v38, v39
	v_cvt_pk_bf16_f32 v36, v36, v37
	v_cvt_pk_bf16_f32 v37, v42, v43
	v_cvt_pk_bf16_f32 v39, v44, v45
	global_store_dwordx4 v[52:53], v[36:39], off offset:256
	s_nop 1
	v_add_u32_e32 v36, 0xa0, v146
	v_mad_i64_i32 v[36:37], s[18:19], v36, s24, v[142:143]
	v_pk_mul_f32 v[38:39], v[30:31], v[242:243] op_sel_hi:[1,0]
	v_pk_mul_f32 v[30:31], v[28:29], v[242:243] op_sel_hi:[1,0]
	v_pk_mul_f32 v[28:29], v[32:33], v[242:243] op_sel_hi:[1,0]
	v_lshl_add_u64 v[36:37], v[36:37], 0, v[144:145]
	v_cvt_pk_bf16_f32 v28, v28, v29
	v_cvt_pk_bf16_f32 v29, v34, v35
	v_cvt_pk_bf16_f32 v30, v30, v31
	v_cvt_pk_bf16_f32 v31, v38, v39
	global_store_dwordx4 v[36:37], v[28:31], off
	s_nop 1
	v_pk_mul_f32 v[28:29], v[22:23], v[242:243] op_sel_hi:[1,0]
	v_pk_mul_f32 v[22:23], v[20:21], v[242:243] op_sel_hi:[1,0]
	v_pk_mul_f32 v[20:21], v[24:25], v[242:243] op_sel_hi:[1,0]
	v_cvt_pk_bf16_f32 v22, v22, v23
	v_cvt_pk_bf16_f32 v20, v20, v21
	v_cvt_pk_bf16_f32 v21, v26, v27
	v_cvt_pk_bf16_f32 v23, v28, v29
	global_store_dwordx4 v[36:37], v[20:23], off offset:256
	s_nop 1
	v_add_u32_e32 v20, 0xb0, v146
	v_mad_i64_i32 v[20:21], s[18:19], v20, s24, v[142:143]
	v_pk_mul_f32 v[22:23], v[14:15], v[244:245] op_sel_hi:[1,0]
	v_pk_mul_f32 v[14:15], v[12:13], v[244:245] op_sel_hi:[1,0]
	v_pk_mul_f32 v[12:13], v[16:17], v[244:245] op_sel_hi:[1,0]
	v_lshl_add_u64 v[20:21], v[20:21], 0, v[144:145]
	v_cvt_pk_bf16_f32 v12, v12, v13
	v_cvt_pk_bf16_f32 v13, v18, v19
	v_cvt_pk_bf16_f32 v14, v14, v15
	v_cvt_pk_bf16_f32 v15, v22, v23
	global_store_dwordx4 v[20:21], v[12:15], off
	s_mov_b64 s[18:19], -1
	s_nop 0
	v_pk_mul_f32 v[12:13], v[6:7], v[244:245] op_sel_hi:[1,0]
	v_pk_mul_f32 v[6:7], v[4:5], v[244:245] op_sel_hi:[1,0]
	v_pk_mul_f32 v[4:5], v[8:9], v[244:245] op_sel_hi:[1,0]
	v_cvt_pk_bf16_f32 v6, v6, v7
	v_cvt_pk_bf16_f32 v4, v4, v5
	v_cvt_pk_bf16_f32 v5, v10, v11
	v_cvt_pk_bf16_f32 v7, v12, v13
	global_store_dwordx4 v[20:21], v[4:7], off offset:256
	s_cbranch_vccnz .LBB0_187
	s_andn2_b64 vcc, exec, s[0:1]
	s_cbranch_vccnz .LBB0_186
	s_barrier
	s_branch .LBB0_186

.LBB0_1829:
	v_readfirstlane_b32 s10, v1
	s_ashr_i32 s30, s10, 6
	s_cmpk_gt_i32 s4, 0x57f
	s_waitcnt vmcnt(0) lgkmcnt(0)
	s_barrier
	s_cbranch_scc1 .LBB0_1845
	s_mov_b32 s101, -1
	v_writelane_b32 v255, s101, 12
	s_mov_b32 s100, s4
	s_cmp_lg_u32 s28, 0x100
	s_cbranch_scc1 .Lgate_u0_std
	s_cmpk_lt_i32 s4, 0x80
	s_cbranch_scc1 .Lgate_u0_std
	s_or_b32 s100, s4, 8
	s_bitcmp1_b32 s4, 3
	s_cselect_b32 s101, 0, 0x200
	s_add_i32 s100, s100, s101

.LBB0_1835:
	v_readlane_b32 s100, v255, 12
	s_cmp_eq_u32 s100, s20
	s_cbranch_scc1 .Lrf_have_gate
	v_writelane_b32 v255, s20, 12
	v_lshl_add_u32 v246, s20, 8, v151
	v_ashrrev_i32_e32 v247, 31, v246
	v_lshl_add_u64 v[246:247], v[246:247], 2, s[6:7]
	global_load_dword v222, v[246:247], off
	global_load_dword v224, v[246:247], off offset:64
	global_load_dword v232, v[246:247], off offset:128
	global_load_dword v234, v[246:247], off offset:192
	global_load_dword v236, v[246:247], off offset:512
	global_load_dword v238, v[246:247], off offset:576
	global_load_dword v242, v[246:247], off offset:640
	global_load_dword v244, v[246:247], off offset:704

.LBB0_1841:
	v_lshl_add_u32 v146, s20, 8, v151
	v_ashrrev_i32_e32 v147, 31, v146
	v_lshl_add_u64 v[148:149], v[146:147], 2, s[6:7]
	v_lshl_or_b32 v144, s21, 8, v154
	v_ashrrev_i32_e32 v145, 31, v144
	v_mov_b64_e32 v[142:143], s[8:9]
	s_movk_i32 s13, 0x2c00
	v_mad_i64_i32 v[158:159], s[20:21], v146, s13, v[142:143]
	v_lshlrev_b64 v[144:145], 1, v[144:145]
	v_lshl_add_u64 v[158:159], v[158:159], 0, v[144:145]
	s_andn2_b64 vcc, exec, s[36:37]
	s_waitcnt lgkmcnt(0)
	v_pk_mul_f32 v[114:115], v[114:115], v[224:225] op_sel_hi:[1,0]
	v_pk_mul_f32 v[106:107], v[106:107], v[224:225] op_sel_hi:[1,0]
	v_pk_mul_f32 v[98:99], v[98:99], v[232:233] op_sel_hi:[1,0]
	v_pk_mul_f32 v[162:163], v[126:127], v[222:223] op_sel_hi:[1,0]
	v_pk_mul_f32 v[126:127], v[124:125], v[222:223] op_sel_hi:[1,0]
	v_pk_mul_f32 v[130:131], v[130:131], v[222:223] op_sel_hi:[1,0]
	v_pk_mul_f32 v[124:125], v[128:129], v[222:223] op_sel_hi:[1,0]
	v_cvt_pk_bf16_f32 v126, v126, v127
	v_cvt_pk_bf16_f32 v124, v124, v125
	v_cvt_pk_bf16_f32 v125, v130, v131
	v_cvt_pk_bf16_f32 v127, v162, v163
	global_store_dwordx4 v[158:159], v[124:127], off
	v_pk_mul_f32 v[122:123], v[122:123], v[222:223] op_sel_hi:[1,0]
	v_pk_mul_f32 v[90:91], v[90:91], v[232:233] op_sel_hi:[1,0]
	v_pk_mul_f32 v[124:125], v[118:119], v[222:223] op_sel_hi:[1,0]
	v_pk_mul_f32 v[118:119], v[116:117], v[222:223] op_sel_hi:[1,0]
	v_pk_mul_f32 v[116:117], v[120:121], v[222:223] op_sel_hi:[1,0]
	v_cvt_pk_bf16_f32 v118, v118, v119
	v_cvt_pk_bf16_f32 v116, v116, v117
	v_cvt_pk_bf16_f32 v117, v122, v123
	v_cvt_pk_bf16_f32 v119, v124, v125
	global_store_dwordx4 v[158:159], v[116:119], off offset:256
	v_pk_mul_f32 v[82:83], v[82:83], v[234:235] op_sel_hi:[1,0]
	v_pk_mul_f32 v[74:75], v[74:75], v[234:235] op_sel_hi:[1,0]
	v_or_b32_e32 v116, 16, v146
	v_mad_i64_i32 v[116:117], s[20:21], v116, s13, v[142:143]
	v_pk_mul_f32 v[118:119], v[110:111], v[224:225] op_sel_hi:[1,0]
	v_pk_mul_f32 v[110:111], v[108:109], v[224:225] op_sel_hi:[1,0]
	v_pk_mul_f32 v[108:109], v[112:113], v[224:225] op_sel_hi:[1,0]
	v_lshl_add_u64 v[116:117], v[116:117], 0, v[144:145]
	v_cvt_pk_bf16_f32 v108, v108, v109
	v_cvt_pk_bf16_f32 v109, v114, v115
	v_cvt_pk_bf16_f32 v110, v110, v111
	v_cvt_pk_bf16_f32 v111, v118, v119
	global_store_dwordx4 v[116:117], v[108:111], off
	s_nop 1
	v_pk_mul_f32 v[108:109], v[102:103], v[224:225] op_sel_hi:[1,0]
	v_pk_mul_f32 v[102:103], v[100:101], v[224:225] op_sel_hi:[1,0]
	v_pk_mul_f32 v[100:101], v[104:105], v[224:225] op_sel_hi:[1,0]
	v_cvt_pk_bf16_f32 v102, v102, v103
	v_cvt_pk_bf16_f32 v100, v100, v101
	v_cvt_pk_bf16_f32 v101, v106, v107
	v_cvt_pk_bf16_f32 v103, v108, v109
	global_store_dwordx4 v[116:117], v[100:103], off offset:256
	s_nop 1
	v_or_b32_e32 v100, 32, v146
	v_mad_i64_i32 v[100:101], s[20:21], v100, s13, v[142:143]
	v_pk_mul_f32 v[102:103], v[94:95], v[232:233] op_sel_hi:[1,0]
	v_pk_mul_f32 v[94:95], v[92:93], v[232:233] op_sel_hi:[1,0]
	v_pk_mul_f32 v[92:93], v[96:97], v[232:233] op_sel_hi:[1,0]
	v_lshl_add_u64 v[100:101], v[100:101], 0, v[144:145]
	v_cvt_pk_bf16_f32 v92, v92, v93
	v_cvt_pk_bf16_f32 v93, v98, v99
	v_cvt_pk_bf16_f32 v94, v94, v95
	v_cvt_pk_bf16_f32 v95, v102, v103
	global_store_dwordx4 v[100:101], v[92:95], off
	s_nop 1
	v_pk_mul_f32 v[92:93], v[86:87], v[232:233] op_sel_hi:[1,0]
	v_pk_mul_f32 v[86:87], v[84:85], v[232:233] op_sel_hi:[1,0]
	v_pk_mul_f32 v[84:85], v[88:89], v[232:233] op_sel_hi:[1,0]
	v_cvt_pk_bf16_f32 v86, v86, v87
	v_cvt_pk_bf16_f32 v84, v84, v85
	v_cvt_pk_bf16_f32 v85, v90, v91
	v_cvt_pk_bf16_f32 v87, v92, v93
	global_store_dwordx4 v[100:101], v[84:87], off offset:256
	s_nop 1
	v_or_b32_e32 v84, 48, v146
	v_mad_i64_i32 v[84:85], s[20:21], v84, s13, v[142:143]
	v_pk_mul_f32 v[86:87], v[78:79], v[234:235] op_sel_hi:[1,0]
	v_pk_mul_f32 v[78:79], v[76:77], v[234:235] op_sel_hi:[1,0]
	v_pk_mul_f32 v[76:77], v[80:81], v[234:235] op_sel_hi:[1,0]
	v_lshl_add_u64 v[84:85], v[84:85], 0, v[144:145]
	v_cvt_pk_bf16_f32 v76, v76, v77
	v_cvt_pk_bf16_f32 v77, v82, v83
	v_cvt_pk_bf16_f32 v78, v78, v79
	v_cvt_pk_bf16_f32 v79, v86, v87
	global_store_dwordx4 v[84:85], v[76:79], off
	s_nop 1
	v_pk_mul_f32 v[76:77], v[70:71], v[234:235] op_sel_hi:[1,0]
	v_pk_mul_f32 v[70:71], v[68:69], v[234:235] op_sel_hi:[1,0]
	v_pk_mul_f32 v[68:69], v[72:73], v[234:235] op_sel_hi:[1,0]
	v_cvt_pk_bf16_f32 v70, v70, v71
	v_cvt_pk_bf16_f32 v68, v68, v69
	v_cvt_pk_bf16_f32 v69, v74, v75
	v_cvt_pk_bf16_f32 v71, v76, v77
	global_store_dwordx4 v[84:85], v[68:71], off offset:256
	s_nop 0
	v_add_u32_e32 v69, 0x80, v146
	v_mad_i64_i32 v[74:75], s[20:21], v69, s13, v[142:143]
	v_lshl_add_u64 v[74:75], v[74:75], 0, v[144:145]
	s_waitcnt lgkmcnt(0)
	v_pk_mul_f32 v[50:51], v[50:51], v[238:239] op_sel_hi:[1,0]
	v_pk_mul_f32 v[42:43], v[42:43], v[238:239] op_sel_hi:[1,0]
	v_pk_mul_f32 v[34:35], v[34:35], v[242:243] op_sel_hi:[1,0]
	v_pk_mul_f32 v[78:79], v[62:63], v[236:237] op_sel_hi:[1,0]
	v_pk_mul_f32 v[62:63], v[60:61], v[236:237] op_sel_hi:[1,0]
	v_pk_mul_f32 v[66:67], v[66:67], v[236:237] op_sel_hi:[1,0]
	v_pk_mul_f32 v[60:61], v[64:65], v[236:237] op_sel_hi:[1,0]
	v_cvt_pk_bf16_f32 v62, v62, v63
	v_cvt_pk_bf16_f32 v60, v60, v61
	v_cvt_pk_bf16_f32 v61, v66, v67
	v_cvt_pk_bf16_f32 v63, v78, v79
	global_store_dwordx4 v[74:75], v[60:63], off
	v_pk_mul_f32 v[58:59], v[58:59], v[236:237] op_sel_hi:[1,0]
	v_pk_mul_f32 v[26:27], v[26:27], v[242:243] op_sel_hi:[1,0]
	v_pk_mul_f32 v[60:61], v[54:55], v[236:237] op_sel_hi:[1,0]
	v_pk_mul_f32 v[54:55], v[52:53], v[236:237] op_sel_hi:[1,0]
	v_pk_mul_f32 v[52:53], v[56:57], v[236:237] op_sel_hi:[1,0]
	v_cvt_pk_bf16_f32 v54, v54, v55
	v_cvt_pk_bf16_f32 v52, v52, v53
	v_cvt_pk_bf16_f32 v53, v58, v59
	v_cvt_pk_bf16_f32 v55, v60, v61
	global_store_dwordx4 v[74:75], v[52:55], off offset:256
	v_pk_mul_f32 v[18:19], v[18:19], v[244:245] op_sel_hi:[1,0]
	v_pk_mul_f32 v[10:11], v[10:11], v[244:245] op_sel_hi:[1,0]
	v_add_u32_e32 v52, 0x90, v146
	v_mad_i64_i32 v[52:53], s[20:21], v52, s13, v[142:143]
	v_pk_mul_f32 v[54:55], v[46:47], v[238:239] op_sel_hi:[1,0]
	v_pk_mul_f32 v[46:47], v[44:45], v[238:239] op_sel_hi:[1,0]
	v_pk_mul_f32 v[44:45], v[48:49], v[238:239] op_sel_hi:[1,0]
	v_lshl_add_u64 v[52:53], v[52:53], 0, v[144:145]
	v_cvt_pk_bf16_f32 v44, v44, v45
	v_cvt_pk_bf16_f32 v45, v50, v51
	v_cvt_pk_bf16_f32 v46, v46, v47
	v_cvt_pk_bf16_f32 v47, v54, v55
	global_store_dwordx4 v[52:53], v[44:47], off
	s_nop 1
	v_pk_mul_f32 v[44:45], v[38:39], v[238:239] op_sel_hi:[1,0]
	v_pk_mul_f32 v[38:39], v[36:37], v[238:239] op_sel_hi:[1,0]
	v_pk_mul_f32 v[36:37], v[40:41], v[238:239] op_sel_hi:[1,0]
	v_cvt_pk_bf16_f32 v38, v38, v39
	v_cvt_pk_bf16_f32 v36, v36, v37
	v_cvt_pk_bf16_f32 v37, v42, v43
	v_cvt_pk_bf16_f32 v39, v44, v45
	global_store_dwordx4 v[52:53], v[36:39], off offset:256
	s_nop 1
	v_add_u32_e32 v36, 0xa0, v146
	v_mad_i64_i32 v[36:37], s[20:21], v36, s13, v[142:143]
	v_pk_mul_f32 v[38:39], v[30:31], v[242:243] op_sel_hi:[1,0]
	v_pk_mul_f32 v[30:31], v[28:29], v[242:243] op_sel_hi:[1,0]
	v_pk_mul_f32 v[28:29], v[32:33], v[242:243] op_sel_hi:[1,0]
	v_lshl_add_u64 v[36:37], v[36:37], 0, v[144:145]
	v_cvt_pk_bf16_f32 v28, v28, v29
	v_cvt_pk_bf16_f32 v29, v34, v35
	v_cvt_pk_bf16_f32 v30, v30, v31
	v_cvt_pk_bf16_f32 v31, v38, v39
	global_store_dwordx4 v[36:37], v[28:31], off
	s_nop 1
	v_pk_mul_f32 v[28:29], v[22:23], v[242:243] op_sel_hi:[1,0]
	v_pk_mul_f32 v[22:23], v[20:21], v[242:243] op_sel_hi:[1,0]
	v_pk_mul_f32 v[20:21], v[24:25], v[242:243] op_sel_hi:[1,0]
	v_cvt_pk_bf16_f32 v22, v22, v23
	v_cvt_pk_bf16_f32 v20, v20, v21
	v_cvt_pk_bf16_f32 v21, v26, v27
	v_cvt_pk_bf16_f32 v23, v28, v29
	global_store_dwordx4 v[36:37], v[20:23], off offset:256
	s_nop 1
	v_add_u32_e32 v20, 0xb0, v146
	v_mad_i64_i32 v[20:21], s[20:21], v20, s13, v[142:143]
	v_pk_mul_f32 v[22:23], v[14:15], v[244:245] op_sel_hi:[1,0]
	v_pk_mul_f32 v[14:15], v[12:13], v[244:245] op_sel_hi:[1,0]
	v_pk_mul_f32 v[12:13], v[16:17], v[244:245] op_sel_hi:[1,0]
	v_lshl_add_u64 v[20:21], v[20:21], 0, v[144:145]
	v_cvt_pk_bf16_f32 v12, v12, v13
	v_cvt_pk_bf16_f32 v13, v18, v19
	v_cvt_pk_bf16_f32 v14, v14, v15
	v_cvt_pk_bf16_f32 v15, v22, v23
	global_store_dwordx4 v[20:21], v[12:15], off
	s_mov_b64 s[20:21], -1
	s_nop 0
	v_pk_mul_f32 v[12:13], v[6:7], v[244:245] op_sel_hi:[1,0]
	v_pk_mul_f32 v[6:7], v[4:5], v[244:245] op_sel_hi:[1,0]
	v_pk_mul_f32 v[4:5], v[8:9], v[244:245] op_sel_hi:[1,0]
	v_cvt_pk_bf16_f32 v6, v6, v7
	v_cvt_pk_bf16_f32 v4, v4, v5
	v_cvt_pk_bf16_f32 v5, v10, v11
	v_cvt_pk_bf16_f32 v7, v12, v13
	global_store_dwordx4 v[20:21], v[4:7], off offset:256
	s_cbranch_vccnz .LBB0_1834
	s_andn2_b64 vcc, exec, s[0:1]
	s_cbranch_vccnz .LBB0_1833
	s_barrier
	s_branch .LBB0_1833
